# code placement: 16-byte pad before the MoE K-loop preheader (loop head at the same 64-byte phase as in the baseline)
# speedup vs baseline: 1.0016x; 1.0016x over previous
.Lmoe_rows_direct:
	v_mov_b32_e32 v248, v134
	v_mov_b32_e32 v249, v136
	v_mov_b32_e32 v250, v138
	v_mov_b32_e32 v223, v140
	s_nop 0
	s_nop 0
	s_nop 0
	s_nop 0
